# combo7 + expert conversion job order permuted: a workgroup's 8 waves take 4 adjacent column blocks x 2 row blocks (1 KB contiguous source rows)
# speedup vs baseline: 1.0376x; 1.0079x over previous
.LBB0_211:
	v_readfirstlane_b32 s38, v0
	s_lshr_b32 s10, s38, 6
	s_lshl_b32 s36, s3, 3
	s_cmpk_lg_i32 s3, 0x100
	s_cselect_b64 s[4:5], -1, 0
	s_cmpk_eq_i32 s3, 0x100
	s_cselect_b64 s[6:7], -1, 0
	s_lshl_b32 s8, s2, 3
	s_add_i32 s37, s10, s8
	s_cmp_lt_i32 s37, 0x12000
	s_cselect_b64 s[8:9], -1, 0
	s_or_b64 s[6:7], s[6:7], s[8:9]
	s_and_b64 s[6:7], s[6:7], exec
	s_cselect_b32 s11, s37, -1
	v_lshlrev_b32_e32 v2, 1, v0
	v_and_b32_e32 v2, 48, v2
	v_lshrrev_b32_e32 v86, 2, v0
	v_and_b32_e32 v86, 8, v86
	v_or_b32_e32 v2, v2, v86
	v_bfe_u32 v86, v0, 5, 1
	v_mad_u32_u24 v86, v86, 56, v2
	v_mov_b32_e32 v87, 0
	s_cmp_lt_i32 s11, 0
	s_barrier
	s_cbranch_scc1 .LBB0_237
	s_cmpk_gt_u32 s11, 0xbfff
	s_cbranch_scc1 .Ljobperm_a_c2
	s_and_b32 s6, s11, 7
	s_lshr_b32 s7, s11, 3
	s_and_b32 s8, s7, 3
	s_lshr_b32 s7, s7, 2
	s_mul_hi_u32 s9, s7, 0xaaaaaaab
	s_lshr_b32 s9, s9, 2
	s_mul_i32 s22, s9, 6
	s_sub_i32 s22, s7, s22
	s_mul_i32 s9, s9, 24
	s_lshl_b32 s22, s22, 2
	s_add_i32 s9, s9, s22
	s_lshr_b32 s22, s6, 1
	s_add_i32 s9, s9, s22
	s_lshl_b32 s9, s9, 3
	s_and_b32 s6, s6, 1
	s_lshl_b32 s8, s8, 1
	s_or_b32 s6, s6, s8
	s_or_b32 s11, s9, s6
	s_branch .Ljobperm_a_done
.Ljobperm_a_c2:
	s_add_i32 s23, s11, 0xffff4000
	s_and_b32 s6, s23, 7
	s_lshr_b32 s7, s23, 3
	s_and_b32 s8, s7, 1
	s_lshr_b32 s7, s7, 1
	s_and_b32 s22, s7, 7
	s_lshr_b32 s9, s7, 3
	s_lshl_b32 s9, s9, 5
	s_lshl_b32 s22, s22, 2
	s_add_i32 s9, s9, s22
	s_lshr_b32 s22, s6, 1
	s_add_i32 s9, s9, s22
	s_lshl_b32 s9, s9, 2
	s_and_b32 s6, s6, 1
	s_lshl_b32 s8, s8, 1
	s_or_b32 s6, s6, s8
	s_or_b32 s9, s9, s6
	s_add_i32 s11, s9, 0xc000
.Ljobperm_a_done:
	s_cmpk_gt_u32 s11, 0xbfff
	s_cbranch_scc0 .LBB0_214
	s_add_i32 s6, s11, 0xffff4000
	s_lshr_b32 s7, s6, 7
	s_mul_hi_u32 s8, s7, 0x55555556
	s_mul_i32 s8, s8, 3
	s_mul_hi_u32 s6, s6, 0xaaaaaaab
	s_sub_i32 s22, s7, s8
	s_lshr_b32 s8, s6, 8
	s_load_dwordx2 s[6:7], s[0:1], 0xa0
	s_load_dwordx2 s[20:21], s[0:1], 0xb0
	s_mul_i32 s24, s8, 0x600000
	s_mul_hi_u32 s23, s8, 0x600000
	s_mov_b32 s9, 0
	s_waitcnt lgkmcnt(0)
	s_add_u32 s6, s6, s24
	s_addc_u32 s7, s7, s23
	s_lshl_b32 s23, s11, 6
	s_lshl_b32 s22, s22, 8
	s_and_b32 s23, s23, 0xc0
	s_or_b32 s22, s22, s23
	s_lshl_b32 s23, s22, 13
	s_add_u32 s6, s6, s23
	s_addc_u32 s7, s7, 0
	s_lshl_b32 s23, s11, 4
	s_and_b32 s23, s23, 0x7c0
	s_lshl_b32 s24, s23, 2
	s_add_u32 s6, s6, s24
	s_addc_u32 s7, s7, 0
	s_lshl_b64 s[8:9], s[8:9], 11
	s_or_b32 s8, s8, s23
	s_mul_i32 s23, s8, 0x300
	s_mul_hi_u32 s8, s8, 0x300
	s_mulk_i32 s9, 0x300
	s_add_i32 s8, s8, s9
	s_add_u32 s9, s20, s23
	s_addc_u32 s8, s21, s8
	s_add_u32 s9, s9, s22
	s_addc_u32 s8, s8, 0
	s_add_u32 s24, s9, 0x1b80a000
	s_addc_u32 s25, s8, 0
	s_mov_b64 s[8:9], 0
	s_branch .LBB0_215

.LBB0_226:
	s_cmp_gt_i32 s79, -1
	s_cselect_b64 s[28:29], -1, 0
	s_cmp_lt_i32 s79, 0
	s_cselect_b64 s[30:31], -1, 0
	s_and_b64 vcc, exec, s[30:31]
	s_mov_b64 s[26:27], s[24:25]
	s_mov_b32 s8, s61
	s_mov_b32 s35, s63
	s_cbranch_vccnz .LBB0_233
	s_cmpk_gt_u32 s79, 0xbfff
	s_cbranch_scc1 .Ljobperm_b_c2
	s_and_b32 s6, s79, 7
	s_lshr_b32 s7, s79, 3
	s_and_b32 s26, s7, 3
	s_lshr_b32 s7, s7, 2
	s_mul_hi_u32 s27, s7, 0xaaaaaaab
	s_lshr_b32 s27, s27, 2
	s_mul_i32 s34, s27, 6
	s_sub_i32 s34, s7, s34
	s_mul_i32 s27, s27, 24
	s_lshl_b32 s34, s34, 2
	s_add_i32 s27, s27, s34
	s_lshr_b32 s34, s6, 1
	s_add_i32 s27, s27, s34
	s_lshl_b32 s27, s27, 3
	s_and_b32 s6, s6, 1
	s_lshl_b32 s26, s26, 1
	s_or_b32 s6, s6, s26
	s_or_b32 s79, s27, s6
	s_branch .Ljobperm_b_done
.Ljobperm_b_c2:
	s_add_i32 s35, s79, 0xffff4000
	s_and_b32 s6, s35, 7
	s_lshr_b32 s7, s35, 3
	s_and_b32 s26, s7, 1
	s_lshr_b32 s7, s7, 1
	s_and_b32 s34, s7, 7
	s_lshr_b32 s27, s7, 3
	s_lshl_b32 s27, s27, 5
	s_lshl_b32 s34, s34, 2
	s_add_i32 s27, s27, s34
	s_lshr_b32 s34, s6, 1
	s_add_i32 s27, s27, s34
	s_lshl_b32 s27, s27, 2
	s_and_b32 s6, s6, 1
	s_lshl_b32 s26, s26, 1
	s_or_b32 s6, s6, s26
	s_or_b32 s27, s27, s6
	s_add_i32 s79, s27, 0xc000
.Ljobperm_b_done:
	s_cmpk_gt_u32 s79, 0xbfff
	s_mov_b64 s[34:35], -1
	s_cbranch_scc0 .LBB0_229
	s_add_i32 s6, s79, 0xffff4000
	s_lshr_b32 s7, s6, 7
	s_mul_hi_u32 s8, s7, 0x55555556
	s_mul_i32 s8, s8, 3
	s_mul_hi_u32 s6, s6, 0xaaaaaaab
	s_sub_i32 s7, s7, s8
	s_lshr_b32 s8, s6, 8
	s_mul_i32 s26, s8, 0x600000
	s_mul_hi_u32 s6, s8, 0x600000
	s_add_u32 s26, s22, s26
	s_addc_u32 s6, s23, s6
	s_lshl_b32 s27, s79, 6
	s_lshl_b32 s7, s7, 8
	s_and_b32 s27, s27, 0xc0
	s_or_b32 s34, s7, s27
	s_lshl_b32 s7, s34, 13
	s_add_u32 s7, s26, s7
	s_addc_u32 s26, s6, 0
	s_lshl_b32 s6, s79, 4
	s_and_b32 s35, s6, 0x7c0
	s_lshl_b32 s6, s35, 2
	s_add_u32 s6, s7, s6
	s_addc_u32 s7, s26, 0
	s_lshl_b64 s[26:27], s[8:9], 11
	s_or_b32 s8, s26, s35
	s_mul_i32 s26, s8, 0x300
	s_mul_hi_u32 s8, s8, 0x300
	s_mulk_i32 s27, 0x300
	s_add_i32 s8, s8, s27
	s_add_u32 s26, s70, s26
	s_addc_u32 s8, s71, s8
	s_add_u32 s26, s26, s34
	s_addc_u32 s27, s8, 0
	s_mov_b64 s[34:35], 0
